# v64 + nt hint on both the loads and the stores of the P0 bf16 weight transposes (all one-shot P0 streams non-temporal)
# baseline (speedup 1.0000x reference)
.LBB0_13:
	s_add_i32 s6, s58, 0xfffff900
	s_cmpk_lt_u32 s6, 0x6000
	s_cbranch_scc1 .LBB0_12
	s_cmpk_gt_i32 s58, 0x4ff
	s_mov_b64 s[2:3], -1
	s_cbranch_scc0 .LBB0_36
	s_cmpk_gt_u32 s58, 0x57f
	s_cbranch_scc0 .LBB0_33
	s_cmpk_gt_u32 s58, 0x5ff
	s_cbranch_scc0 .LBB0_30
	s_cmpk_gt_u32 s58, 0x6ff
	s_cbranch_scc0 .LBB0_27
	s_cmpk_gt_u32 s58, 0x46ff
	s_cbranch_scc0 .LBB0_24
	s_cmpk_gt_u32 s58, 0x66ff
	s_cbranch_scc0 .LBB0_21
	s_add_i32 s0, s58, 0xffff9900
	s_lshr_b32 s0, s0, 5
	s_lshl_b64 s[2:3], s[0:1], 19
	s_lshl_b64 s[60:61], s[0:1], 18
	s_add_u32 s0, s12, s60
	s_addc_u32 s7, s13, s61
	s_and_b32 s33, s16, 0x7c0
	v_or_b32_e32 v4, s33, v105
	v_lshl_add_u64 v[2:3], v[72:73], 0, s[2:3]
	v_lshlrev_b32_e32 v70, 8, v4
	v_lshl_add_u64 v[50:51], v[2:3], 0, v[70:71]
	s_movk_i32 s2, 0x1000
	v_add_co_u32_e32 v30, vcc, s2, v50
	s_movk_i32 s2, 0x2000
	s_nop 0
	v_addc_co_u32_e32 v31, vcc, 0, v51, vcc
	v_add_co_u32_e32 v46, vcc, s2, v50
	s_movk_i32 s2, 0x3000
	s_nop 0
	v_addc_co_u32_e32 v47, vcc, 0, v51, vcc
	v_add_co_u32_e32 v62, vcc, s2, v50
	global_load_dwordx4 v[2:5], v[50:51], off nt
	global_load_dwordx4 v[6:9], v[50:51], off offset:1024 nt
	global_load_dwordx4 v[10:13], v[50:51], off offset:2048 nt
	global_load_dwordx4 v[14:17], v[50:51], off offset:3072 nt
	v_addc_co_u32_e32 v63, vcc, 0, v51, vcc
	global_load_dwordx4 v[18:21], v[46:47], off offset:-4096 nt
	global_load_dwordx4 v[22:25], v[30:31], off offset:1024 nt
	global_load_dwordx4 v[26:29], v[30:31], off offset:2048 nt
	s_nop 0
	global_load_dwordx4 v[30:33], v[30:31], off offset:3072 nt
	s_nop 0
	global_load_dwordx4 v[34:37], v[46:47], off nt
	global_load_dwordx4 v[38:41], v[46:47], off offset:1024 nt
	global_load_dwordx4 v[42:45], v[46:47], off offset:2048 nt
	s_nop 0
	global_load_dwordx4 v[46:49], v[46:47], off offset:3072 nt
	s_nop 0
	global_load_dwordx4 v[50:53], v[62:63], off nt
	global_load_dwordx4 v[54:57], v[62:63], off offset:1024 nt
	global_load_dwordx4 v[58:61], v[62:63], off offset:2048 nt
	s_nop 0
	global_load_dwordx4 v[62:65], v[62:63], off offset:3072 nt
	s_lshl_b32 s2, s33, 1
	s_add_u32 s2, s0, s2
	s_addc_u32 s3, s7, 0
	v_mov_b32_e32 v101, v71
	s_waitcnt vmcnt(14)
	ds_write2_b32 v106, v2, v6 offset1:4
	ds_write2_b32 v106, v3, v7 offset0:65 offset1:69
	ds_write2_b32 v106, v4, v8 offset0:130 offset1:134
	ds_write2_b32 v106, v5, v9 offset0:195 offset1:199
	s_waitcnt vmcnt(12)
	ds_write2_b32 v106, v10, v14 offset0:8 offset1:12
	ds_write2_b32 v106, v11, v15 offset0:73 offset1:77
	ds_write2_b32 v106, v12, v16 offset0:138 offset1:142
	ds_write2_b32 v106, v13, v17 offset0:203 offset1:207
	s_waitcnt vmcnt(10)
	ds_write2_b32 v106, v18, v22 offset0:16 offset1:20
	ds_write2_b32 v106, v19, v23 offset0:81 offset1:85
	ds_write2_b32 v106, v20, v24 offset0:146 offset1:150
	ds_write2_b32 v106, v21, v25 offset0:211 offset1:215
	s_waitcnt vmcnt(8)
	ds_write2_b32 v106, v26, v30 offset0:24 offset1:28
	ds_write2_b32 v106, v27, v31 offset0:89 offset1:93
	ds_write2_b32 v106, v28, v32 offset0:154 offset1:158
	ds_write2_b32 v106, v29, v33 offset0:219 offset1:223
	s_waitcnt vmcnt(6)
	ds_write2_b32 v106, v34, v38 offset0:32 offset1:36
	ds_write2_b32 v106, v35, v39 offset0:97 offset1:101
	ds_write2_b32 v106, v36, v40 offset0:162 offset1:166
	ds_write2_b32 v106, v37, v41 offset0:227 offset1:231
	s_waitcnt vmcnt(4)
	ds_write2_b32 v106, v42, v46 offset0:40 offset1:44
	ds_write2_b32 v106, v43, v47 offset0:105 offset1:109
	ds_write2_b32 v106, v44, v48 offset0:170 offset1:174
	ds_write2_b32 v106, v45, v49 offset0:235 offset1:239
	s_waitcnt vmcnt(2)
	ds_write2_b32 v106, v50, v54 offset0:48 offset1:52
	ds_write2_b32 v106, v51, v55 offset0:113 offset1:117
	ds_write2_b32 v106, v52, v56 offset0:178 offset1:182
	ds_write2_b32 v106, v53, v57 offset0:243 offset1:247
	s_waitcnt vmcnt(0)
	ds_write2_b32 v106, v58, v62 offset0:56 offset1:60
	ds_write2_b32 v106, v59, v63 offset0:121 offset1:125
	ds_write2_b32 v106, v60, v64 offset0:186 offset1:190
	ds_write2_b32 v106, v61, v65 offset0:251 offset1:255
	s_waitcnt lgkmcnt(0)
	ds_read2_b32 v[2:3], v118 offset1:1
	ds_read2_b32 v[4:5], v118 offset0:2 offset1:3
	ds_read2_b32 v[8:9], v118 offset0:6 offset1:7
	v_lshl_add_u64 v[6:7], s[2:3], 0, v[100:101]
	s_mov_b64 s[2:3], 0
	s_waitcnt lgkmcnt(2)
	v_cvt_pk_bf16_f32 v2, v2, v3
	s_waitcnt lgkmcnt(1)
	v_cvt_pk_bf16_f32 v3, v4, v5
	ds_read2_b32 v[4:5], v118 offset0:4 offset1:5
	s_waitcnt lgkmcnt(0)
	v_cvt_pk_bf16_f32 v4, v4, v5
	v_cvt_pk_bf16_f32 v5, v8, v9
	v_lshl_add_u64 v[8:9], v[6:7], 0, v[74:75]
	global_store_dwordx4 v[8:9], v[2:5], off nt
	ds_read2_b32 v[2:3], v119 offset1:1
	ds_read2_b32 v[4:5], v120 offset1:1
	ds_read2_b32 v[8:9], v122 offset1:1
	s_waitcnt lgkmcnt(2)
	v_cvt_pk_bf16_f32 v2, v2, v3
	s_waitcnt lgkmcnt(1)
	v_cvt_pk_bf16_f32 v3, v4, v5
	ds_read2_b32 v[4:5], v121 offset1:1
	s_waitcnt lgkmcnt(0)
	v_cvt_pk_bf16_f32 v4, v4, v5
	v_cvt_pk_bf16_f32 v5, v8, v9
	v_lshl_add_u64 v[8:9], v[6:7], 0, v[76:77]
	global_store_dwordx4 v[8:9], v[2:5], off nt
	ds_read2_b32 v[2:3], v123 offset1:1
	ds_read2_b32 v[4:5], v124 offset1:1
	s_waitcnt lgkmcnt(1)
	v_cvt_pk_bf16_f32 v2, v2, v3
	s_waitcnt lgkmcnt(0)
	v_cvt_pk_bf16_f32 v3, v4, v5
	ds_read2_b32 v[4:5], v125 offset1:1
	s_waitcnt lgkmcnt(0)
	v_cvt_pk_bf16_f32 v4, v4, v5
	v_add_u32_e32 v5, 0x1058, v118
	ds_read2_b32 v[8:9], v5 offset1:1
	s_waitcnt lgkmcnt(0)
	v_cvt_pk_bf16_f32 v5, v8, v9
	v_lshl_add_u64 v[8:9], v[6:7], 0, v[78:79]
	global_store_dwordx4 v[8:9], v[2:5], off nt
	s_nop 1
	v_add_u32_e32 v2, 0x1860, v118
	ds_read2_b32 v[2:3], v2 offset1:1
	s_waitcnt lgkmcnt(0)
	v_cvt_pk_bf16_f32 v2, v2, v3
	v_add_u32_e32 v3, 0x1868, v118
	ds_read2_b32 v[4:5], v3 offset1:1
	s_waitcnt lgkmcnt(0)
	v_cvt_pk_bf16_f32 v3, v4, v5
	v_add_u32_e32 v4, 0x1870, v118
	ds_read2_b32 v[4:5], v4 offset1:1
	s_waitcnt lgkmcnt(0)
	v_cvt_pk_bf16_f32 v4, v4, v5
	v_add_u32_e32 v5, 0x1878, v118
	ds_read2_b32 v[8:9], v5 offset1:1
	s_waitcnt lgkmcnt(0)
	v_cvt_pk_bf16_f32 v5, v8, v9
	v_lshl_add_u64 v[8:9], v[6:7], 0, v[80:81]
	global_store_dwordx4 v[8:9], v[2:5], off nt
	s_nop 1
	v_add_u32_e32 v2, 0x2080, v118
	ds_read2_b32 v[2:3], v2 offset1:1
	s_waitcnt lgkmcnt(0)
	v_cvt_pk_bf16_f32 v2, v2, v3
	v_add_u32_e32 v3, 0x2088, v118
	ds_read2_b32 v[4:5], v3 offset1:1
	s_waitcnt lgkmcnt(0)
	v_cvt_pk_bf16_f32 v3, v4, v5
	v_add_u32_e32 v4, 0x2090, v118
	ds_read2_b32 v[4:5], v4 offset1:1
	s_waitcnt lgkmcnt(0)
	v_cvt_pk_bf16_f32 v4, v4, v5
	v_add_u32_e32 v5, 0x2098, v118
	ds_read2_b32 v[8:9], v5 offset1:1
	s_waitcnt lgkmcnt(0)
	v_cvt_pk_bf16_f32 v5, v8, v9
	v_lshl_add_u64 v[8:9], v[6:7], 0, v[82:83]
	global_store_dwordx4 v[8:9], v[2:5], off nt
	s_nop 1
	v_add_u32_e32 v2, 0x28a0, v118
	ds_read2_b32 v[2:3], v2 offset1:1
	s_waitcnt lgkmcnt(0)
	v_cvt_pk_bf16_f32 v2, v2, v3
	v_add_u32_e32 v3, 0x28a8, v118
	ds_read2_b32 v[4:5], v3 offset1:1
	s_waitcnt lgkmcnt(0)
	v_cvt_pk_bf16_f32 v3, v4, v5
	v_add_u32_e32 v4, 0x28b0, v118
	ds_read2_b32 v[4:5], v4 offset1:1
	s_waitcnt lgkmcnt(0)
	v_cvt_pk_bf16_f32 v4, v4, v5
	v_add_u32_e32 v5, 0x28b8, v118
	ds_read2_b32 v[8:9], v5 offset1:1
	s_waitcnt lgkmcnt(0)
	v_cvt_pk_bf16_f32 v5, v8, v9
	v_lshl_add_u64 v[8:9], v[6:7], 0, v[84:85]
	global_store_dwordx4 v[8:9], v[2:5], off nt
	s_nop 1
	v_add_u32_e32 v2, 0x30c0, v118
	ds_read2_b32 v[2:3], v2 offset1:1
	s_waitcnt lgkmcnt(0)
	v_cvt_pk_bf16_f32 v2, v2, v3
	v_add_u32_e32 v3, 0x30c8, v118
	ds_read2_b32 v[4:5], v3 offset1:1
	s_waitcnt lgkmcnt(0)
	v_cvt_pk_bf16_f32 v3, v4, v5
	v_add_u32_e32 v4, 0x30d0, v118
	ds_read2_b32 v[4:5], v4 offset1:1
	s_waitcnt lgkmcnt(0)
	v_cvt_pk_bf16_f32 v4, v4, v5
	v_add_u32_e32 v5, 0x30d8, v118
	ds_read2_b32 v[8:9], v5 offset1:1
	s_waitcnt lgkmcnt(0)
	v_cvt_pk_bf16_f32 v5, v8, v9
	v_lshl_add_u64 v[8:9], v[6:7], 0, v[86:87]
	global_store_dwordx4 v[8:9], v[2:5], off nt
	v_lshl_add_u64 v[6:7], v[6:7], 0, v[88:89]
	s_nop 0
	v_add_u32_e32 v2, 0x38e0, v118
	ds_read2_b32 v[2:3], v2 offset1:1
	s_waitcnt lgkmcnt(0)
	v_cvt_pk_bf16_f32 v2, v2, v3
	v_add_u32_e32 v3, 0x38e8, v118
	ds_read2_b32 v[4:5], v3 offset1:1
	s_waitcnt lgkmcnt(0)
	v_cvt_pk_bf16_f32 v3, v4, v5
	v_add_u32_e32 v4, 0x38f0, v118
	ds_read2_b32 v[4:5], v4 offset1:1
	s_waitcnt lgkmcnt(0)
	v_cvt_pk_bf16_f32 v4, v4, v5
	v_add_u32_e32 v5, 0x38f8, v118
	ds_read2_b32 v[8:9], v5 offset1:1
	s_waitcnt lgkmcnt(0)
	v_cvt_pk_bf16_f32 v5, v8, v9
	global_store_dwordx4 v[6:7], v[2:5], off nt
	s_waitcnt lgkmcnt(0)

.LBB0_27:
	s_andn2_b64 vcc, exec, s[2:3]
	s_cbranch_vccnz .LBB0_29
	s_and_b32 s0, s18, 0x1fc0
	s_and_b32 s2, s16, 0x3c0
	s_addk_i32 s0, 0xe800
	v_or_b32_e32 v2, s2, v67
	v_readlane_b32 s60, v255, 3
	v_or_b32_e32 v58, s0, v105
	v_lshlrev_b32_e32 v70, 2, v2
	v_readlane_b32 s64, v255, 7
	v_readlane_b32 s65, v255, 8
	v_mov_b32_e32 v59, v71
	v_lshlrev_b64 v[2:3], 12, v[58:59]
	v_lshl_add_u64 v[60:61], s[64:65], 0, v[70:71]
	v_or_b32_e32 v70, 4, v58
	v_lshlrev_b64 v[4:5], 12, v[70:71]
	v_or_b32_e32 v70, 8, v58
	v_lshlrev_b64 v[10:11], 12, v[70:71]
	v_or_b32_e32 v70, 12, v58
	v_lshlrev_b64 v[12:13], 12, v[70:71]
	v_or_b32_e32 v70, 16, v58
	v_lshlrev_b64 v[18:19], 12, v[70:71]
	v_or_b32_e32 v70, 20, v58
	v_lshlrev_b64 v[20:21], 12, v[70:71]
	v_or_b32_e32 v70, 24, v58
	v_lshlrev_b64 v[26:27], 12, v[70:71]
	v_or_b32_e32 v70, 28, v58
	v_lshlrev_b64 v[28:29], 12, v[70:71]
	v_or_b32_e32 v70, 32, v58
	v_lshlrev_b64 v[34:35], 12, v[70:71]
	v_or_b32_e32 v70, 36, v58
	v_lshlrev_b64 v[36:37], 12, v[70:71]
	v_or_b32_e32 v70, 40, v58
	v_lshlrev_b64 v[42:43], 12, v[70:71]
	v_or_b32_e32 v70, 44, v58
	v_lshlrev_b64 v[44:45], 12, v[70:71]
	v_or_b32_e32 v70, 48, v58
	v_lshlrev_b64 v[50:51], 12, v[70:71]
	v_or_b32_e32 v70, 52, v58
	v_lshlrev_b64 v[52:53], 12, v[70:71]
	v_or_b32_e32 v70, 56, v58
	v_lshlrev_b64 v[62:63], 12, v[70:71]
	v_or_b32_e32 v70, 60, v58
	v_lshlrev_b64 v[58:59], 12, v[70:71]
	v_lshl_add_u64 v[2:3], v[60:61], 0, v[2:3]
	v_lshl_add_u64 v[6:7], v[60:61], 0, v[4:5]
	v_lshl_add_u64 v[10:11], v[60:61], 0, v[10:11]
	v_lshl_add_u64 v[14:15], v[60:61], 0, v[12:13]
	v_lshl_add_u64 v[18:19], v[60:61], 0, v[18:19]
	v_lshl_add_u64 v[22:23], v[60:61], 0, v[20:21]
	v_lshl_add_u64 v[26:27], v[60:61], 0, v[26:27]
	v_lshl_add_u64 v[30:31], v[60:61], 0, v[28:29]
	v_lshl_add_u64 v[34:35], v[60:61], 0, v[34:35]
	v_lshl_add_u64 v[38:39], v[60:61], 0, v[36:37]
	v_lshl_add_u64 v[42:43], v[60:61], 0, v[42:43]
	v_lshl_add_u64 v[46:47], v[60:61], 0, v[44:45]
	v_lshl_add_u64 v[50:51], v[60:61], 0, v[50:51]
	v_lshl_add_u64 v[54:55], v[60:61], 0, v[52:53]
	v_lshl_add_u64 v[62:63], v[60:61], 0, v[62:63]
	v_lshl_add_u64 v[64:65], v[60:61], 0, v[58:59]
	global_load_dwordx4 v[2:5], v[2:3], off nt
	s_nop 0
	global_load_dwordx4 v[6:9], v[6:7], off nt
	s_nop 0
	global_load_dwordx4 v[10:13], v[10:11], off nt
	s_nop 0
	global_load_dwordx4 v[14:17], v[14:15], off nt
	s_nop 0
	global_load_dwordx4 v[18:21], v[18:19], off nt
	s_nop 0
	global_load_dwordx4 v[22:25], v[22:23], off nt
	s_nop 0
	global_load_dwordx4 v[26:29], v[26:27], off nt
	s_nop 0
	global_load_dwordx4 v[30:33], v[30:31], off nt
	s_nop 0
	global_load_dwordx4 v[34:37], v[34:35], off nt
	s_nop 0
	global_load_dwordx4 v[38:41], v[38:39], off nt
	s_nop 0
	global_load_dwordx4 v[42:45], v[42:43], off nt
	s_nop 0
	global_load_dwordx4 v[46:49], v[46:47], off nt
	s_nop 0
	global_load_dwordx4 v[50:53], v[50:51], off nt
	s_nop 0
	global_load_dwordx4 v[54:57], v[54:55], off nt
	s_nop 0
	global_load_dwordx4 v[58:61], v[62:63], off nt
	s_nop 0
	global_load_dwordx4 v[62:65], v[64:65], off nt
	v_readlane_b32 s61, v255, 4
	v_readlane_b32 s62, v255, 5
	v_readlane_b32 s63, v255, 6
	v_readlane_b32 s66, v255, 9
	v_readlane_b32 s67, v255, 10
	v_readlane_b32 s68, v255, 11
	v_readlane_b32 s69, v255, 12
	v_readlane_b32 s70, v255, 13
	v_readlane_b32 s71, v255, 14
	v_readlane_b32 s72, v255, 15
	v_readlane_b32 s73, v255, 16
	v_readlane_b32 s74, v255, 17
	v_readlane_b32 s75, v255, 18
	s_waitcnt vmcnt(14)
	ds_write2_b32 v106, v2, v6 offset1:4
	ds_write2_b32 v106, v3, v7 offset0:65 offset1:69
	ds_write2_b32 v106, v4, v8 offset0:130 offset1:134
	ds_write2_b32 v106, v5, v9 offset0:195 offset1:199
	s_waitcnt vmcnt(12)
	ds_write2_b32 v106, v10, v14 offset0:8 offset1:12
	ds_write2_b32 v106, v11, v15 offset0:73 offset1:77
	ds_write2_b32 v106, v12, v16 offset0:138 offset1:142
	ds_write2_b32 v106, v13, v17 offset0:203 offset1:207
	s_waitcnt vmcnt(10)
	ds_write2_b32 v106, v18, v22 offset0:16 offset1:20
	ds_write2_b32 v106, v19, v23 offset0:81 offset1:85
	ds_write2_b32 v106, v20, v24 offset0:146 offset1:150
	ds_write2_b32 v106, v21, v25 offset0:211 offset1:215
	s_waitcnt vmcnt(8)
	ds_write2_b32 v106, v26, v30 offset0:24 offset1:28
	ds_write2_b32 v106, v27, v31 offset0:89 offset1:93
	ds_write2_b32 v106, v28, v32 offset0:154 offset1:158
	ds_write2_b32 v106, v29, v33 offset0:219 offset1:223
	s_waitcnt vmcnt(6)
	ds_write2_b32 v106, v34, v38 offset0:32 offset1:36
	ds_write2_b32 v106, v35, v39 offset0:97 offset1:101
	ds_write2_b32 v106, v36, v40 offset0:162 offset1:166
	ds_write2_b32 v106, v37, v41 offset0:227 offset1:231
	s_waitcnt vmcnt(4)
	ds_write2_b32 v106, v42, v46 offset0:40 offset1:44
	ds_write2_b32 v106, v43, v47 offset0:105 offset1:109
	ds_write2_b32 v106, v44, v48 offset0:170 offset1:174
	ds_write2_b32 v106, v45, v49 offset0:235 offset1:239
	s_waitcnt vmcnt(2)
	ds_write2_b32 v106, v50, v54 offset0:48 offset1:52
	ds_write2_b32 v106, v51, v55 offset0:113 offset1:117
	ds_write2_b32 v106, v52, v56 offset0:178 offset1:182
	ds_write2_b32 v106, v53, v57 offset0:243 offset1:247
	s_waitcnt vmcnt(0)
	ds_write2_b32 v106, v58, v62 offset0:56 offset1:60
	ds_write2_b32 v106, v59, v63 offset0:121 offset1:125
	ds_write2_b32 v106, v60, v64 offset0:186 offset1:190
	ds_write2_b32 v106, v61, v65 offset0:251 offset1:255
	s_waitcnt lgkmcnt(0)
	ds_read2_b32 v[2:3], v118 offset1:1
	ds_read2_b32 v[4:5], v118 offset0:2 offset1:3
	ds_read2_b32 v[6:7], v118 offset0:4 offset1:5
	ds_read2_b32 v[8:9], v118 offset0:6 offset1:7
	v_lshl_add_u64 v[10:11], s[0:1], 1, v[92:93]
	s_waitcnt lgkmcnt(3)
	v_cvt_pk_bf16_f32 v2, v2, v3
	s_waitcnt lgkmcnt(2)
	v_cvt_pk_bf16_f32 v3, v4, v5
	s_waitcnt lgkmcnt(1)
	v_cvt_pk_bf16_f32 v4, v6, v7
	s_waitcnt lgkmcnt(0)
	v_cvt_pk_bf16_f32 v5, v8, v9
	ds_read2_b32 v[8:9], v119 offset1:1
	ds_read2_b32 v[12:13], v120 offset1:1
	ds_read2_b32 v[14:15], v121 offset1:1
	ds_read2_b32 v[16:17], v122 offset1:1
	v_or_b32_e32 v6, s2, v107
	v_lshlrev_b32_e32 v70, 11, v6
	v_lshl_add_u64 v[6:7], v[10:11], 0, v[70:71]
	global_store_dwordx4 v[6:7], v[2:5], off nt
	v_or_b32_e32 v6, s2, v108
	v_lshlrev_b32_e32 v70, 11, v6
	s_waitcnt lgkmcnt(0)
	v_cvt_pk_bf16_f32 v5, v16, v17
	v_add_u32_e32 v16, 0x1058, v118
	v_cvt_pk_bf16_f32 v2, v8, v9
	v_cvt_pk_bf16_f32 v3, v12, v13
	v_cvt_pk_bf16_f32 v4, v14, v15
	ds_read2_b32 v[8:9], v123 offset1:1
	ds_read2_b32 v[12:13], v124 offset1:1
	ds_read2_b32 v[14:15], v125 offset1:1
	ds_read2_b32 v[16:17], v16 offset1:1
	v_lshl_add_u64 v[6:7], v[10:11], 0, v[70:71]
	global_store_dwordx4 v[6:7], v[2:5], off nt
	v_or_b32_e32 v6, s2, v109
	v_lshlrev_b32_e32 v70, 11, v6
	s_waitcnt lgkmcnt(3)
	v_cvt_pk_bf16_f32 v2, v8, v9
	s_waitcnt lgkmcnt(2)
	v_cvt_pk_bf16_f32 v3, v12, v13
	s_waitcnt lgkmcnt(1)
	v_cvt_pk_bf16_f32 v4, v14, v15
	s_waitcnt lgkmcnt(0)
	v_cvt_pk_bf16_f32 v5, v16, v17
	v_add_u32_e32 v8, 0x1860, v118
	v_add_u32_e32 v12, 0x1868, v118
	v_add_u32_e32 v14, 0x1870, v118
	v_add_u32_e32 v16, 0x1878, v118
	ds_read2_b32 v[8:9], v8 offset1:1
	ds_read2_b32 v[12:13], v12 offset1:1
	ds_read2_b32 v[14:15], v14 offset1:1
	ds_read2_b32 v[16:17], v16 offset1:1
	v_lshl_add_u64 v[6:7], v[10:11], 0, v[70:71]
	global_store_dwordx4 v[6:7], v[2:5], off nt
	v_or_b32_e32 v6, s2, v110
	v_lshlrev_b32_e32 v70, 11, v6
	s_waitcnt lgkmcnt(3)
	v_cvt_pk_bf16_f32 v2, v8, v9
	s_waitcnt lgkmcnt(2)
	v_cvt_pk_bf16_f32 v3, v12, v13
	s_waitcnt lgkmcnt(1)
	v_cvt_pk_bf16_f32 v4, v14, v15
	s_waitcnt lgkmcnt(0)
	v_cvt_pk_bf16_f32 v5, v16, v17
	v_add_u32_e32 v8, 0x2080, v118
	v_add_u32_e32 v12, 0x2088, v118
	v_add_u32_e32 v14, 0x2090, v118
	v_add_u32_e32 v16, 0x2098, v118
	ds_read2_b32 v[8:9], v8 offset1:1
	ds_read2_b32 v[12:13], v12 offset1:1
	ds_read2_b32 v[14:15], v14 offset1:1
	ds_read2_b32 v[16:17], v16 offset1:1
	v_lshl_add_u64 v[6:7], v[10:11], 0, v[70:71]
	global_store_dwordx4 v[6:7], v[2:5], off nt
	v_or_b32_e32 v6, s2, v111
	v_lshlrev_b32_e32 v70, 11, v6
	s_waitcnt lgkmcnt(3)
	v_cvt_pk_bf16_f32 v2, v8, v9
	s_waitcnt lgkmcnt(2)
	v_cvt_pk_bf16_f32 v3, v12, v13
	s_waitcnt lgkmcnt(1)
	v_cvt_pk_bf16_f32 v4, v14, v15
	s_waitcnt lgkmcnt(0)
	v_cvt_pk_bf16_f32 v5, v16, v17
	v_add_u32_e32 v8, 0x28a0, v118
	v_add_u32_e32 v12, 0x28a8, v118
	v_add_u32_e32 v14, 0x28b0, v118
	v_add_u32_e32 v16, 0x28b8, v118
	ds_read2_b32 v[8:9], v8 offset1:1
	ds_read2_b32 v[12:13], v12 offset1:1
	ds_read2_b32 v[14:15], v14 offset1:1
	ds_read2_b32 v[16:17], v16 offset1:1
	v_lshl_add_u64 v[6:7], v[10:11], 0, v[70:71]
	global_store_dwordx4 v[6:7], v[2:5], off nt
	v_or_b32_e32 v6, s2, v112
	v_lshlrev_b32_e32 v70, 11, v6
	s_waitcnt lgkmcnt(3)
	v_cvt_pk_bf16_f32 v2, v8, v9
	s_waitcnt lgkmcnt(2)
	v_cvt_pk_bf16_f32 v3, v12, v13
	s_waitcnt lgkmcnt(1)
	v_cvt_pk_bf16_f32 v4, v14, v15
	s_waitcnt lgkmcnt(0)
	v_cvt_pk_bf16_f32 v5, v16, v17
	v_add_u32_e32 v8, 0x30c0, v118
	v_add_u32_e32 v12, 0x30c8, v118
	v_add_u32_e32 v14, 0x30d0, v118
	v_add_u32_e32 v16, 0x30d8, v118
	ds_read2_b32 v[8:9], v8 offset1:1
	ds_read2_b32 v[12:13], v12 offset1:1
	ds_read2_b32 v[14:15], v14 offset1:1
	ds_read2_b32 v[16:17], v16 offset1:1
	v_lshl_add_u64 v[6:7], v[10:11], 0, v[70:71]
	global_store_dwordx4 v[6:7], v[2:5], off nt
	v_or_b32_e32 v6, s2, v113
	v_lshlrev_b32_e32 v70, 11, v6
	s_waitcnt lgkmcnt(3)
	v_cvt_pk_bf16_f32 v2, v8, v9
	s_waitcnt lgkmcnt(2)
	v_cvt_pk_bf16_f32 v3, v12, v13
	s_waitcnt lgkmcnt(1)
	v_cvt_pk_bf16_f32 v4, v14, v15
	s_waitcnt lgkmcnt(0)
	v_cvt_pk_bf16_f32 v5, v16, v17
	v_add_u32_e32 v8, 0x38e0, v118
	v_add_u32_e32 v12, 0x38e8, v118
	v_add_u32_e32 v14, 0x38f0, v118
	v_add_u32_e32 v16, 0x38f8, v118
	ds_read2_b32 v[8:9], v8 offset1:1
	ds_read2_b32 v[12:13], v12 offset1:1
	ds_read2_b32 v[14:15], v14 offset1:1
	ds_read2_b32 v[16:17], v16 offset1:1
	v_lshl_add_u64 v[6:7], v[10:11], 0, v[70:71]
	global_store_dwordx4 v[6:7], v[2:5], off nt
	v_or_b32_e32 v6, s2, v114
	v_lshlrev_b32_e32 v70, 11, v6
	s_waitcnt lgkmcnt(3)
	v_cvt_pk_bf16_f32 v2, v8, v9
	s_waitcnt lgkmcnt(2)
	v_cvt_pk_bf16_f32 v3, v12, v13
	s_waitcnt lgkmcnt(1)
	v_cvt_pk_bf16_f32 v4, v14, v15
	s_waitcnt lgkmcnt(0)
	v_cvt_pk_bf16_f32 v5, v16, v17
	v_lshl_add_u64 v[6:7], v[10:11], 0, v[70:71]
	global_store_dwordx4 v[6:7], v[2:5], off nt
	s_waitcnt lgkmcnt(0)

.LBB0_30:
	s_andn2_b64 vcc, exec, s[2:3]
	s_cbranch_vccnz .LBB0_32
	s_and_b32 s0, s18, 0x1fc0
	s_and_b32 s2, s16, 0x3c0
	s_addk_i32 s0, 0xea00
	v_or_b32_e32 v2, s2, v67
	v_readlane_b32 s60, v255, 3
	v_or_b32_e32 v58, s0, v105
	v_lshlrev_b32_e32 v70, 2, v2
	v_readlane_b32 s62, v255, 5
	v_readlane_b32 s63, v255, 6
	v_mov_b32_e32 v59, v71
	v_lshlrev_b64 v[2:3], 12, v[58:59]
	v_lshl_add_u64 v[60:61], s[62:63], 0, v[70:71]
	v_or_b32_e32 v70, 4, v58
	v_lshlrev_b64 v[4:5], 12, v[70:71]
	v_or_b32_e32 v70, 8, v58
	v_lshlrev_b64 v[10:11], 12, v[70:71]
	v_or_b32_e32 v70, 12, v58
	v_lshlrev_b64 v[12:13], 12, v[70:71]
	v_or_b32_e32 v70, 16, v58
	v_lshlrev_b64 v[18:19], 12, v[70:71]
	v_or_b32_e32 v70, 20, v58
	v_lshlrev_b64 v[20:21], 12, v[70:71]
	v_or_b32_e32 v70, 24, v58
	v_lshlrev_b64 v[26:27], 12, v[70:71]
	v_or_b32_e32 v70, 28, v58
	v_lshlrev_b64 v[28:29], 12, v[70:71]
	v_or_b32_e32 v70, 32, v58
	v_lshlrev_b64 v[34:35], 12, v[70:71]
	v_or_b32_e32 v70, 36, v58
	v_lshlrev_b64 v[36:37], 12, v[70:71]
	v_or_b32_e32 v70, 40, v58
	v_lshlrev_b64 v[42:43], 12, v[70:71]
	v_or_b32_e32 v70, 44, v58
	v_lshlrev_b64 v[44:45], 12, v[70:71]
	v_or_b32_e32 v70, 48, v58
	v_lshlrev_b64 v[50:51], 12, v[70:71]
	v_or_b32_e32 v70, 52, v58
	v_lshlrev_b64 v[52:53], 12, v[70:71]
	v_or_b32_e32 v70, 56, v58
	v_lshlrev_b64 v[62:63], 12, v[70:71]
	v_or_b32_e32 v70, 60, v58
	v_lshlrev_b64 v[58:59], 12, v[70:71]
	v_lshl_add_u64 v[2:3], v[60:61], 0, v[2:3]
	v_lshl_add_u64 v[6:7], v[60:61], 0, v[4:5]
	v_lshl_add_u64 v[10:11], v[60:61], 0, v[10:11]
	v_lshl_add_u64 v[14:15], v[60:61], 0, v[12:13]
	v_lshl_add_u64 v[18:19], v[60:61], 0, v[18:19]
	v_lshl_add_u64 v[22:23], v[60:61], 0, v[20:21]
	v_lshl_add_u64 v[26:27], v[60:61], 0, v[26:27]
	v_lshl_add_u64 v[30:31], v[60:61], 0, v[28:29]
	v_lshl_add_u64 v[34:35], v[60:61], 0, v[34:35]
	v_lshl_add_u64 v[38:39], v[60:61], 0, v[36:37]
	v_lshl_add_u64 v[42:43], v[60:61], 0, v[42:43]
	v_lshl_add_u64 v[46:47], v[60:61], 0, v[44:45]
	v_lshl_add_u64 v[50:51], v[60:61], 0, v[50:51]
	v_lshl_add_u64 v[54:55], v[60:61], 0, v[52:53]
	v_lshl_add_u64 v[62:63], v[60:61], 0, v[62:63]
	v_lshl_add_u64 v[64:65], v[60:61], 0, v[58:59]
	global_load_dwordx4 v[2:5], v[2:3], off nt
	s_nop 0
	global_load_dwordx4 v[6:9], v[6:7], off nt
	s_nop 0
	global_load_dwordx4 v[10:13], v[10:11], off nt
	s_nop 0
	global_load_dwordx4 v[14:17], v[14:15], off nt
	s_nop 0
	global_load_dwordx4 v[18:21], v[18:19], off nt
	s_nop 0
	global_load_dwordx4 v[22:25], v[22:23], off nt
	s_nop 0
	global_load_dwordx4 v[26:29], v[26:27], off nt
	s_nop 0
	global_load_dwordx4 v[30:33], v[30:31], off nt
	s_nop 0
	global_load_dwordx4 v[34:37], v[34:35], off nt
	s_nop 0
	global_load_dwordx4 v[38:41], v[38:39], off nt
	s_nop 0
	global_load_dwordx4 v[42:45], v[42:43], off nt
	s_nop 0
	global_load_dwordx4 v[46:49], v[46:47], off nt
	s_nop 0
	global_load_dwordx4 v[50:53], v[50:51], off nt
	s_nop 0
	global_load_dwordx4 v[54:57], v[54:55], off nt
	s_nop 0
	global_load_dwordx4 v[58:61], v[62:63], off nt
	s_nop 0
	global_load_dwordx4 v[62:65], v[64:65], off nt
	v_readlane_b32 s61, v255, 4
	v_readlane_b32 s64, v255, 7
	v_readlane_b32 s65, v255, 8
	v_readlane_b32 s66, v255, 9
	v_readlane_b32 s67, v255, 10
	v_readlane_b32 s68, v255, 11
	v_readlane_b32 s69, v255, 12
	v_readlane_b32 s70, v255, 13
	v_readlane_b32 s71, v255, 14
	v_readlane_b32 s72, v255, 15
	v_readlane_b32 s73, v255, 16
	v_readlane_b32 s74, v255, 17
	v_readlane_b32 s75, v255, 18
	s_waitcnt vmcnt(14)
	ds_write2_b32 v106, v2, v6 offset1:4
	ds_write2_b32 v106, v3, v7 offset0:65 offset1:69
	ds_write2_b32 v106, v4, v8 offset0:130 offset1:134
	ds_write2_b32 v106, v5, v9 offset0:195 offset1:199
	s_waitcnt vmcnt(12)
	ds_write2_b32 v106, v10, v14 offset0:8 offset1:12
	ds_write2_b32 v106, v11, v15 offset0:73 offset1:77
	ds_write2_b32 v106, v12, v16 offset0:138 offset1:142
	ds_write2_b32 v106, v13, v17 offset0:203 offset1:207
	s_waitcnt vmcnt(10)
	ds_write2_b32 v106, v18, v22 offset0:16 offset1:20
	ds_write2_b32 v106, v19, v23 offset0:81 offset1:85
	ds_write2_b32 v106, v20, v24 offset0:146 offset1:150
	ds_write2_b32 v106, v21, v25 offset0:211 offset1:215
	s_waitcnt vmcnt(8)
	ds_write2_b32 v106, v26, v30 offset0:24 offset1:28
	ds_write2_b32 v106, v27, v31 offset0:89 offset1:93
	ds_write2_b32 v106, v28, v32 offset0:154 offset1:158
	ds_write2_b32 v106, v29, v33 offset0:219 offset1:223
	s_waitcnt vmcnt(6)
	ds_write2_b32 v106, v34, v38 offset0:32 offset1:36
	ds_write2_b32 v106, v35, v39 offset0:97 offset1:101
	ds_write2_b32 v106, v36, v40 offset0:162 offset1:166
	ds_write2_b32 v106, v37, v41 offset0:227 offset1:231
	s_waitcnt vmcnt(4)
	ds_write2_b32 v106, v42, v46 offset0:40 offset1:44
	ds_write2_b32 v106, v43, v47 offset0:105 offset1:109
	ds_write2_b32 v106, v44, v48 offset0:170 offset1:174
	ds_write2_b32 v106, v45, v49 offset0:235 offset1:239
	s_waitcnt vmcnt(2)
	ds_write2_b32 v106, v50, v54 offset0:48 offset1:52
	ds_write2_b32 v106, v51, v55 offset0:113 offset1:117
	ds_write2_b32 v106, v52, v56 offset0:178 offset1:182
	ds_write2_b32 v106, v53, v57 offset0:243 offset1:247
	s_waitcnt vmcnt(0)
	ds_write2_b32 v106, v58, v62 offset0:56 offset1:60
	ds_write2_b32 v106, v59, v63 offset0:121 offset1:125
	ds_write2_b32 v106, v60, v64 offset0:186 offset1:190
	ds_write2_b32 v106, v61, v65 offset0:251 offset1:255
	s_waitcnt lgkmcnt(0)
	ds_read2_b32 v[2:3], v118 offset1:1
	ds_read2_b32 v[4:5], v118 offset0:2 offset1:3
	ds_read2_b32 v[6:7], v118 offset0:4 offset1:5
	ds_read2_b32 v[8:9], v118 offset0:6 offset1:7
	v_lshl_add_u64 v[10:11], s[0:1], 1, v[94:95]
	s_waitcnt lgkmcnt(3)
	v_cvt_pk_bf16_f32 v2, v2, v3
	s_waitcnt lgkmcnt(2)
	v_cvt_pk_bf16_f32 v3, v4, v5
	s_waitcnt lgkmcnt(1)
	v_cvt_pk_bf16_f32 v4, v6, v7
	s_waitcnt lgkmcnt(0)
	v_cvt_pk_bf16_f32 v5, v8, v9
	ds_read2_b32 v[8:9], v119 offset1:1
	ds_read2_b32 v[12:13], v120 offset1:1
	ds_read2_b32 v[14:15], v121 offset1:1
	ds_read2_b32 v[16:17], v122 offset1:1
	v_or_b32_e32 v6, s2, v107
	v_lshlrev_b32_e32 v70, 11, v6
	v_lshl_add_u64 v[6:7], v[10:11], 0, v[70:71]
	global_store_dwordx4 v[6:7], v[2:5], off nt
	v_or_b32_e32 v6, s2, v108
	v_lshlrev_b32_e32 v70, 11, v6
	s_waitcnt lgkmcnt(0)
	v_cvt_pk_bf16_f32 v5, v16, v17
	v_add_u32_e32 v16, 0x1058, v118
	v_cvt_pk_bf16_f32 v2, v8, v9
	v_cvt_pk_bf16_f32 v3, v12, v13
	v_cvt_pk_bf16_f32 v4, v14, v15
	ds_read2_b32 v[8:9], v123 offset1:1
	ds_read2_b32 v[12:13], v124 offset1:1
	ds_read2_b32 v[14:15], v125 offset1:1
	ds_read2_b32 v[16:17], v16 offset1:1
	v_lshl_add_u64 v[6:7], v[10:11], 0, v[70:71]
	global_store_dwordx4 v[6:7], v[2:5], off nt
	v_or_b32_e32 v6, s2, v109
	v_lshlrev_b32_e32 v70, 11, v6
	s_waitcnt lgkmcnt(3)
	v_cvt_pk_bf16_f32 v2, v8, v9
	s_waitcnt lgkmcnt(2)
	v_cvt_pk_bf16_f32 v3, v12, v13
	s_waitcnt lgkmcnt(1)
	v_cvt_pk_bf16_f32 v4, v14, v15
	s_waitcnt lgkmcnt(0)
	v_cvt_pk_bf16_f32 v5, v16, v17
	v_add_u32_e32 v8, 0x1860, v118
	v_add_u32_e32 v12, 0x1868, v118
	v_add_u32_e32 v14, 0x1870, v118
	v_add_u32_e32 v16, 0x1878, v118
	ds_read2_b32 v[8:9], v8 offset1:1
	ds_read2_b32 v[12:13], v12 offset1:1
	ds_read2_b32 v[14:15], v14 offset1:1
	ds_read2_b32 v[16:17], v16 offset1:1
	v_lshl_add_u64 v[6:7], v[10:11], 0, v[70:71]
	global_store_dwordx4 v[6:7], v[2:5], off nt
	v_or_b32_e32 v6, s2, v110
	v_lshlrev_b32_e32 v70, 11, v6
	s_waitcnt lgkmcnt(3)
	v_cvt_pk_bf16_f32 v2, v8, v9
	s_waitcnt lgkmcnt(2)
	v_cvt_pk_bf16_f32 v3, v12, v13
	s_waitcnt lgkmcnt(1)
	v_cvt_pk_bf16_f32 v4, v14, v15
	s_waitcnt lgkmcnt(0)
	v_cvt_pk_bf16_f32 v5, v16, v17
	v_add_u32_e32 v8, 0x2080, v118
	v_add_u32_e32 v12, 0x2088, v118
	v_add_u32_e32 v14, 0x2090, v118
	v_add_u32_e32 v16, 0x2098, v118
	ds_read2_b32 v[8:9], v8 offset1:1
	ds_read2_b32 v[12:13], v12 offset1:1
	ds_read2_b32 v[14:15], v14 offset1:1
	ds_read2_b32 v[16:17], v16 offset1:1
	v_lshl_add_u64 v[6:7], v[10:11], 0, v[70:71]
	global_store_dwordx4 v[6:7], v[2:5], off nt
	v_or_b32_e32 v6, s2, v111
	v_lshlrev_b32_e32 v70, 11, v6
	s_waitcnt lgkmcnt(3)
	v_cvt_pk_bf16_f32 v2, v8, v9
	s_waitcnt lgkmcnt(2)
	v_cvt_pk_bf16_f32 v3, v12, v13
	s_waitcnt lgkmcnt(1)
	v_cvt_pk_bf16_f32 v4, v14, v15
	s_waitcnt lgkmcnt(0)
	v_cvt_pk_bf16_f32 v5, v16, v17
	v_add_u32_e32 v8, 0x28a0, v118
	v_add_u32_e32 v12, 0x28a8, v118
	v_add_u32_e32 v14, 0x28b0, v118
	v_add_u32_e32 v16, 0x28b8, v118
	ds_read2_b32 v[8:9], v8 offset1:1
	ds_read2_b32 v[12:13], v12 offset1:1
	ds_read2_b32 v[14:15], v14 offset1:1
	ds_read2_b32 v[16:17], v16 offset1:1
	v_lshl_add_u64 v[6:7], v[10:11], 0, v[70:71]
	global_store_dwordx4 v[6:7], v[2:5], off nt
	v_or_b32_e32 v6, s2, v112
	v_lshlrev_b32_e32 v70, 11, v6
	s_waitcnt lgkmcnt(3)
	v_cvt_pk_bf16_f32 v2, v8, v9
	s_waitcnt lgkmcnt(2)
	v_cvt_pk_bf16_f32 v3, v12, v13
	s_waitcnt lgkmcnt(1)
	v_cvt_pk_bf16_f32 v4, v14, v15
	s_waitcnt lgkmcnt(0)
	v_cvt_pk_bf16_f32 v5, v16, v17
	v_add_u32_e32 v8, 0x30c0, v118
	v_add_u32_e32 v12, 0x30c8, v118
	v_add_u32_e32 v14, 0x30d0, v118
	v_add_u32_e32 v16, 0x30d8, v118
	ds_read2_b32 v[8:9], v8 offset1:1
	ds_read2_b32 v[12:13], v12 offset1:1
	ds_read2_b32 v[14:15], v14 offset1:1
	ds_read2_b32 v[16:17], v16 offset1:1
	v_lshl_add_u64 v[6:7], v[10:11], 0, v[70:71]
	global_store_dwordx4 v[6:7], v[2:5], off nt
	v_or_b32_e32 v6, s2, v113
	v_lshlrev_b32_e32 v70, 11, v6
	s_waitcnt lgkmcnt(3)
	v_cvt_pk_bf16_f32 v2, v8, v9
	s_waitcnt lgkmcnt(2)
	v_cvt_pk_bf16_f32 v3, v12, v13
	s_waitcnt lgkmcnt(1)
	v_cvt_pk_bf16_f32 v4, v14, v15
	s_waitcnt lgkmcnt(0)
	v_cvt_pk_bf16_f32 v5, v16, v17
	v_add_u32_e32 v8, 0x38e0, v118
	v_add_u32_e32 v12, 0x38e8, v118
	v_add_u32_e32 v14, 0x38f0, v118
	v_add_u32_e32 v16, 0x38f8, v118
	ds_read2_b32 v[8:9], v8 offset1:1
	ds_read2_b32 v[12:13], v12 offset1:1
	ds_read2_b32 v[14:15], v14 offset1:1
	ds_read2_b32 v[16:17], v16 offset1:1
	v_lshl_add_u64 v[6:7], v[10:11], 0, v[70:71]
	global_store_dwordx4 v[6:7], v[2:5], off nt
	v_or_b32_e32 v6, s2, v114
	v_lshlrev_b32_e32 v70, 11, v6
	s_waitcnt lgkmcnt(3)
	v_cvt_pk_bf16_f32 v2, v8, v9
	s_waitcnt lgkmcnt(2)
	v_cvt_pk_bf16_f32 v3, v12, v13
	s_waitcnt lgkmcnt(1)
	v_cvt_pk_bf16_f32 v4, v14, v15
	s_waitcnt lgkmcnt(0)
	v_cvt_pk_bf16_f32 v5, v16, v17
	v_lshl_add_u64 v[6:7], v[10:11], 0, v[70:71]
	global_store_dwordx4 v[6:7], v[2:5], off nt
	s_waitcnt lgkmcnt(0)

.LBB0_33:
	s_andn2_b64 vcc, exec, s[2:3]
	s_cbranch_vccnz .LBB0_35
	s_and_b32 s0, s18, 0x1fc0
	s_and_b32 s2, s16, 0x3c0
	s_addk_i32 s0, 0xec00
	v_or_b32_e32 v2, s2, v67
	v_readlane_b32 s60, v255, 3
	v_or_b32_e32 v58, s0, v105
	v_lshlrev_b32_e32 v70, 2, v2
	v_readlane_b32 s61, v255, 4
	v_mov_b32_e32 v59, v71
	v_lshlrev_b64 v[2:3], 12, v[58:59]
	v_lshl_add_u64 v[60:61], s[60:61], 0, v[70:71]
	v_or_b32_e32 v70, 4, v58
	v_lshlrev_b64 v[4:5], 12, v[70:71]
	v_or_b32_e32 v70, 8, v58
	v_lshlrev_b64 v[10:11], 12, v[70:71]
	v_or_b32_e32 v70, 12, v58
	v_lshlrev_b64 v[12:13], 12, v[70:71]
	v_or_b32_e32 v70, 16, v58
	v_lshlrev_b64 v[18:19], 12, v[70:71]
	v_or_b32_e32 v70, 20, v58
	v_lshlrev_b64 v[20:21], 12, v[70:71]
	v_or_b32_e32 v70, 24, v58
	v_lshlrev_b64 v[26:27], 12, v[70:71]
	v_or_b32_e32 v70, 28, v58
	v_lshlrev_b64 v[28:29], 12, v[70:71]
	v_or_b32_e32 v70, 32, v58
	v_lshlrev_b64 v[34:35], 12, v[70:71]
	v_or_b32_e32 v70, 36, v58
	v_lshlrev_b64 v[36:37], 12, v[70:71]
	v_or_b32_e32 v70, 40, v58
	v_lshlrev_b64 v[42:43], 12, v[70:71]
	v_or_b32_e32 v70, 44, v58
	v_lshlrev_b64 v[44:45], 12, v[70:71]
	v_or_b32_e32 v70, 48, v58
	v_lshlrev_b64 v[50:51], 12, v[70:71]
	v_or_b32_e32 v70, 52, v58
	v_lshlrev_b64 v[52:53], 12, v[70:71]
	v_or_b32_e32 v70, 56, v58
	v_lshlrev_b64 v[62:63], 12, v[70:71]
	v_or_b32_e32 v70, 60, v58
	v_lshlrev_b64 v[58:59], 12, v[70:71]
	v_lshl_add_u64 v[2:3], v[60:61], 0, v[2:3]
	v_lshl_add_u64 v[6:7], v[60:61], 0, v[4:5]
	v_lshl_add_u64 v[10:11], v[60:61], 0, v[10:11]
	v_lshl_add_u64 v[14:15], v[60:61], 0, v[12:13]
	v_lshl_add_u64 v[18:19], v[60:61], 0, v[18:19]
	v_lshl_add_u64 v[22:23], v[60:61], 0, v[20:21]
	v_lshl_add_u64 v[26:27], v[60:61], 0, v[26:27]
	v_lshl_add_u64 v[30:31], v[60:61], 0, v[28:29]
	v_lshl_add_u64 v[34:35], v[60:61], 0, v[34:35]
	v_lshl_add_u64 v[38:39], v[60:61], 0, v[36:37]
	v_lshl_add_u64 v[42:43], v[60:61], 0, v[42:43]
	v_lshl_add_u64 v[46:47], v[60:61], 0, v[44:45]
	v_lshl_add_u64 v[50:51], v[60:61], 0, v[50:51]
	v_lshl_add_u64 v[54:55], v[60:61], 0, v[52:53]
	v_lshl_add_u64 v[62:63], v[60:61], 0, v[62:63]
	v_lshl_add_u64 v[64:65], v[60:61], 0, v[58:59]
	global_load_dwordx4 v[2:5], v[2:3], off nt
	s_nop 0
	global_load_dwordx4 v[6:9], v[6:7], off nt
	s_nop 0
	global_load_dwordx4 v[10:13], v[10:11], off nt
	s_nop 0
	global_load_dwordx4 v[14:17], v[14:15], off nt
	s_nop 0
	global_load_dwordx4 v[18:21], v[18:19], off nt
	s_nop 0
	global_load_dwordx4 v[22:25], v[22:23], off nt
	s_nop 0
	global_load_dwordx4 v[26:29], v[26:27], off nt
	s_nop 0
	global_load_dwordx4 v[30:33], v[30:31], off nt
	s_nop 0
	global_load_dwordx4 v[34:37], v[34:35], off nt
	s_nop 0
	global_load_dwordx4 v[38:41], v[38:39], off nt
	s_nop 0
	global_load_dwordx4 v[42:45], v[42:43], off nt
	s_nop 0
	global_load_dwordx4 v[46:49], v[46:47], off nt
	s_nop 0
	global_load_dwordx4 v[50:53], v[50:51], off nt
	s_nop 0
	global_load_dwordx4 v[54:57], v[54:55], off nt
	s_nop 0
	global_load_dwordx4 v[58:61], v[62:63], off nt
	s_nop 0
	global_load_dwordx4 v[62:65], v[64:65], off nt
	v_readlane_b32 s62, v255, 5
	v_readlane_b32 s63, v255, 6
	v_readlane_b32 s64, v255, 7
	v_readlane_b32 s65, v255, 8
	v_readlane_b32 s66, v255, 9
	v_readlane_b32 s67, v255, 10
	v_readlane_b32 s68, v255, 11
	v_readlane_b32 s69, v255, 12
	v_readlane_b32 s70, v255, 13
	v_readlane_b32 s71, v255, 14
	v_readlane_b32 s72, v255, 15
	v_readlane_b32 s73, v255, 16
	v_readlane_b32 s74, v255, 17
	v_readlane_b32 s75, v255, 18
	s_waitcnt vmcnt(14)
	ds_write2_b32 v106, v2, v6 offset1:4
	ds_write2_b32 v106, v3, v7 offset0:65 offset1:69
	ds_write2_b32 v106, v4, v8 offset0:130 offset1:134
	ds_write2_b32 v106, v5, v9 offset0:195 offset1:199
	s_waitcnt vmcnt(12)
	ds_write2_b32 v106, v10, v14 offset0:8 offset1:12
	ds_write2_b32 v106, v11, v15 offset0:73 offset1:77
	ds_write2_b32 v106, v12, v16 offset0:138 offset1:142
	ds_write2_b32 v106, v13, v17 offset0:203 offset1:207
	s_waitcnt vmcnt(10)
	ds_write2_b32 v106, v18, v22 offset0:16 offset1:20
	ds_write2_b32 v106, v19, v23 offset0:81 offset1:85
	ds_write2_b32 v106, v20, v24 offset0:146 offset1:150
	ds_write2_b32 v106, v21, v25 offset0:211 offset1:215
	s_waitcnt vmcnt(8)
	ds_write2_b32 v106, v26, v30 offset0:24 offset1:28
	ds_write2_b32 v106, v27, v31 offset0:89 offset1:93
	ds_write2_b32 v106, v28, v32 offset0:154 offset1:158
	ds_write2_b32 v106, v29, v33 offset0:219 offset1:223
	s_waitcnt vmcnt(6)
	ds_write2_b32 v106, v34, v38 offset0:32 offset1:36
	ds_write2_b32 v106, v35, v39 offset0:97 offset1:101
	ds_write2_b32 v106, v36, v40 offset0:162 offset1:166
	ds_write2_b32 v106, v37, v41 offset0:227 offset1:231
	s_waitcnt vmcnt(4)
	ds_write2_b32 v106, v42, v46 offset0:40 offset1:44
	ds_write2_b32 v106, v43, v47 offset0:105 offset1:109
	ds_write2_b32 v106, v44, v48 offset0:170 offset1:174
	ds_write2_b32 v106, v45, v49 offset0:235 offset1:239
	s_waitcnt vmcnt(2)
	ds_write2_b32 v106, v50, v54 offset0:48 offset1:52
	ds_write2_b32 v106, v51, v55 offset0:113 offset1:117
	ds_write2_b32 v106, v52, v56 offset0:178 offset1:182
	ds_write2_b32 v106, v53, v57 offset0:243 offset1:247
	s_waitcnt vmcnt(0)
	ds_write2_b32 v106, v58, v62 offset0:56 offset1:60
	ds_write2_b32 v106, v59, v63 offset0:121 offset1:125
	ds_write2_b32 v106, v60, v64 offset0:186 offset1:190
	ds_write2_b32 v106, v61, v65 offset0:251 offset1:255
	s_waitcnt lgkmcnt(0)
	ds_read2_b32 v[2:3], v118 offset1:1
	ds_read2_b32 v[4:5], v118 offset0:2 offset1:3
	ds_read2_b32 v[6:7], v118 offset0:4 offset1:5
	ds_read2_b32 v[8:9], v118 offset0:6 offset1:7
	v_lshl_add_u64 v[10:11], s[0:1], 1, v[96:97]
	s_waitcnt lgkmcnt(3)
	v_cvt_pk_bf16_f32 v2, v2, v3
	s_waitcnt lgkmcnt(2)
	v_cvt_pk_bf16_f32 v3, v4, v5
	s_waitcnt lgkmcnt(1)
	v_cvt_pk_bf16_f32 v4, v6, v7
	s_waitcnt lgkmcnt(0)
	v_cvt_pk_bf16_f32 v5, v8, v9
	ds_read2_b32 v[8:9], v119 offset1:1
	ds_read2_b32 v[12:13], v120 offset1:1
	ds_read2_b32 v[14:15], v121 offset1:1
	ds_read2_b32 v[16:17], v122 offset1:1
	v_or_b32_e32 v6, s2, v107
	v_lshlrev_b32_e32 v70, 11, v6
	v_lshl_add_u64 v[6:7], v[10:11], 0, v[70:71]
	global_store_dwordx4 v[6:7], v[2:5], off nt
	v_or_b32_e32 v6, s2, v108
	v_lshlrev_b32_e32 v70, 11, v6
	s_waitcnt lgkmcnt(0)
	v_cvt_pk_bf16_f32 v5, v16, v17
	v_add_u32_e32 v16, 0x1058, v118
	v_cvt_pk_bf16_f32 v2, v8, v9
	v_cvt_pk_bf16_f32 v3, v12, v13
	v_cvt_pk_bf16_f32 v4, v14, v15
	ds_read2_b32 v[8:9], v123 offset1:1
	ds_read2_b32 v[12:13], v124 offset1:1
	ds_read2_b32 v[14:15], v125 offset1:1
	ds_read2_b32 v[16:17], v16 offset1:1
	v_lshl_add_u64 v[6:7], v[10:11], 0, v[70:71]
	global_store_dwordx4 v[6:7], v[2:5], off nt
	v_or_b32_e32 v6, s2, v109
	v_lshlrev_b32_e32 v70, 11, v6
	s_waitcnt lgkmcnt(3)
	v_cvt_pk_bf16_f32 v2, v8, v9
	s_waitcnt lgkmcnt(2)
	v_cvt_pk_bf16_f32 v3, v12, v13
	s_waitcnt lgkmcnt(1)
	v_cvt_pk_bf16_f32 v4, v14, v15
	s_waitcnt lgkmcnt(0)
	v_cvt_pk_bf16_f32 v5, v16, v17
	v_add_u32_e32 v8, 0x1860, v118
	v_add_u32_e32 v12, 0x1868, v118
	v_add_u32_e32 v14, 0x1870, v118
	v_add_u32_e32 v16, 0x1878, v118
	ds_read2_b32 v[8:9], v8 offset1:1
	ds_read2_b32 v[12:13], v12 offset1:1
	ds_read2_b32 v[14:15], v14 offset1:1
	ds_read2_b32 v[16:17], v16 offset1:1
	v_lshl_add_u64 v[6:7], v[10:11], 0, v[70:71]
	global_store_dwordx4 v[6:7], v[2:5], off nt
	v_or_b32_e32 v6, s2, v110
	v_lshlrev_b32_e32 v70, 11, v6
	s_waitcnt lgkmcnt(3)
	v_cvt_pk_bf16_f32 v2, v8, v9
	s_waitcnt lgkmcnt(2)
	v_cvt_pk_bf16_f32 v3, v12, v13
	s_waitcnt lgkmcnt(1)
	v_cvt_pk_bf16_f32 v4, v14, v15
	s_waitcnt lgkmcnt(0)
	v_cvt_pk_bf16_f32 v5, v16, v17
	v_add_u32_e32 v8, 0x2080, v118
	v_add_u32_e32 v12, 0x2088, v118
	v_add_u32_e32 v14, 0x2090, v118
	v_add_u32_e32 v16, 0x2098, v118
	ds_read2_b32 v[8:9], v8 offset1:1
	ds_read2_b32 v[12:13], v12 offset1:1
	ds_read2_b32 v[14:15], v14 offset1:1
	ds_read2_b32 v[16:17], v16 offset1:1
	v_lshl_add_u64 v[6:7], v[10:11], 0, v[70:71]
	global_store_dwordx4 v[6:7], v[2:5], off nt
	v_or_b32_e32 v6, s2, v111
	v_lshlrev_b32_e32 v70, 11, v6
	s_waitcnt lgkmcnt(3)
	v_cvt_pk_bf16_f32 v2, v8, v9
	s_waitcnt lgkmcnt(2)
	v_cvt_pk_bf16_f32 v3, v12, v13
	s_waitcnt lgkmcnt(1)
	v_cvt_pk_bf16_f32 v4, v14, v15
	s_waitcnt lgkmcnt(0)
	v_cvt_pk_bf16_f32 v5, v16, v17
	v_add_u32_e32 v8, 0x28a0, v118
	v_add_u32_e32 v12, 0x28a8, v118
	v_add_u32_e32 v14, 0x28b0, v118
	v_add_u32_e32 v16, 0x28b8, v118
	ds_read2_b32 v[8:9], v8 offset1:1
	ds_read2_b32 v[12:13], v12 offset1:1
	ds_read2_b32 v[14:15], v14 offset1:1
	ds_read2_b32 v[16:17], v16 offset1:1
	v_lshl_add_u64 v[6:7], v[10:11], 0, v[70:71]
	global_store_dwordx4 v[6:7], v[2:5], off nt
	v_or_b32_e32 v6, s2, v112
	v_lshlrev_b32_e32 v70, 11, v6
	s_waitcnt lgkmcnt(3)
	v_cvt_pk_bf16_f32 v2, v8, v9
	s_waitcnt lgkmcnt(2)
	v_cvt_pk_bf16_f32 v3, v12, v13
	s_waitcnt lgkmcnt(1)
	v_cvt_pk_bf16_f32 v4, v14, v15
	s_waitcnt lgkmcnt(0)
	v_cvt_pk_bf16_f32 v5, v16, v17
	v_add_u32_e32 v8, 0x30c0, v118
	v_add_u32_e32 v12, 0x30c8, v118
	v_add_u32_e32 v14, 0x30d0, v118
	v_add_u32_e32 v16, 0x30d8, v118
	ds_read2_b32 v[8:9], v8 offset1:1
	ds_read2_b32 v[12:13], v12 offset1:1
	ds_read2_b32 v[14:15], v14 offset1:1
	ds_read2_b32 v[16:17], v16 offset1:1
	v_lshl_add_u64 v[6:7], v[10:11], 0, v[70:71]
	global_store_dwordx4 v[6:7], v[2:5], off nt
	v_or_b32_e32 v6, s2, v113
	v_lshlrev_b32_e32 v70, 11, v6
	s_waitcnt lgkmcnt(3)
	v_cvt_pk_bf16_f32 v2, v8, v9
	s_waitcnt lgkmcnt(2)
	v_cvt_pk_bf16_f32 v3, v12, v13
	s_waitcnt lgkmcnt(1)
	v_cvt_pk_bf16_f32 v4, v14, v15
	s_waitcnt lgkmcnt(0)
	v_cvt_pk_bf16_f32 v5, v16, v17
	v_add_u32_e32 v8, 0x38e0, v118
	v_add_u32_e32 v12, 0x38e8, v118
	v_add_u32_e32 v14, 0x38f0, v118
	v_add_u32_e32 v16, 0x38f8, v118
	ds_read2_b32 v[8:9], v8 offset1:1
	ds_read2_b32 v[12:13], v12 offset1:1
	ds_read2_b32 v[14:15], v14 offset1:1
	ds_read2_b32 v[16:17], v16 offset1:1
	v_lshl_add_u64 v[6:7], v[10:11], 0, v[70:71]
	global_store_dwordx4 v[6:7], v[2:5], off nt
	v_or_b32_e32 v6, s2, v114
	v_lshlrev_b32_e32 v70, 11, v6
	s_waitcnt lgkmcnt(3)
	v_cvt_pk_bf16_f32 v2, v8, v9
	s_waitcnt lgkmcnt(2)
	v_cvt_pk_bf16_f32 v3, v12, v13
	s_waitcnt lgkmcnt(1)
	v_cvt_pk_bf16_f32 v4, v14, v15
	s_waitcnt lgkmcnt(0)
	v_cvt_pk_bf16_f32 v5, v16, v17
	v_lshl_add_u64 v[6:7], v[10:11], 0, v[70:71]
	global_store_dwordx4 v[6:7], v[2:5], off nt
	s_waitcnt lgkmcnt(0)
